# attn P buffer row stride 784 -> 800 bytes (conflict-free ds_read_b128 A fragments in the P.V phase); unused MFMA rows 24-31 re-read rows 16-23
# speedup vs baseline: 1.0092x; 1.0092x over previous
.Lf_27:
	s_or_b64 exec, exec, s[2:3]
	v_and_b32_e32 v2, 0x3f0, v116
	v_add_u32_e32 v166, 0, v2
	s_waitcnt lgkmcnt(0)
	s_barrier
	global_load_dwordx4 v[66:69], v38, s[8:9]
	global_load_dwordx4 v[70:73], v38, s[8:9] offset:16
	global_load_dwordx4 v[74:77], v38, s[8:9] offset:32
	global_load_dwordx4 v[78:81], v38, s[8:9] offset:48
	v_and_b32_e32 v167, 31, v0
	v_lshl_or_b32 v167, s51, 5, v167
	s_mul_i32 s38, s33, 0x1800
	v_add_u32_e32 v2, s38, v167
	v_lshlrev_b32_e32 v2, 5, v2
	v_bfe_u32 v3, v0, 5, 1
	v_lshl_add_u32 v2, v3, 4, v2
	s_mov_b32 s44, s16
	s_mov_b32 s45, s17
	global_load_dwordx4 v[102:105], v2, s[44:45]
	s_add_u32 s44, s44, 0x3000
	s_addc_u32 s45, s45, 0
	global_load_dwordx4 v[106:109], v2, s[44:45]
	s_add_u32 s44, s44, 0x3000
	s_addc_u32 s45, s45, 0
	global_load_dwordx4 v[110:113], v2, s[44:45]
	s_add_u32 s44, s44, 0x3000
	s_addc_u32 s45, s45, 0
	global_load_dwordx4 v[114:117], v2, s[44:45]
	s_add_u32 s44, s44, 0x3000
	s_addc_u32 s45, s45, 0
	global_load_dwordx4 v[118:121], v2, s[44:45]
	s_add_u32 s44, s44, 0x3000
	s_addc_u32 s45, s45, 0
	global_load_dwordx4 v[122:125], v2, s[44:45]
	s_add_u32 s44, s44, 0x3000
	s_addc_u32 s45, s45, 0
	global_load_dwordx4 v[126:129], v2, s[44:45]
	s_add_u32 s44, s44, 0x3000
	s_addc_u32 s45, s45, 0
	global_load_dwordx4 v[130:133], v2, s[44:45]
	s_add_u32 s44, s44, 0x3000
	s_addc_u32 s45, s45, 0
	global_load_dwordx4 v[134:137], v2, s[44:45]
	s_add_u32 s44, s44, 0x3000
	s_addc_u32 s45, s45, 0
	global_load_dwordx4 v[138:141], v2, s[44:45]
	s_add_u32 s44, s44, 0x3000
	s_addc_u32 s45, s45, 0
	global_load_dwordx4 v[142:145], v2, s[44:45]
	s_add_u32 s44, s44, 0x3000
	s_addc_u32 s45, s45, 0
	global_load_dwordx4 v[146:149], v2, s[44:45]
	s_add_u32 s44, s44, 0x3000
	s_addc_u32 s45, s45, 0
	global_load_dwordx4 v[150:153], v2, s[44:45]
	s_add_u32 s44, s44, 0x3000
	s_addc_u32 s45, s45, 0
	global_load_dwordx4 v[154:157], v2, s[44:45]
	s_add_u32 s44, s44, 0x3000
	s_addc_u32 s45, s45, 0
	global_load_dwordx4 v[158:161], v2, s[44:45]
	s_add_u32 s44, s44, 0x3000
	s_addc_u32 s45, s45, 0
	global_load_dwordx4 v[162:165], v2, s[44:45]
	v_mul_u32_u24_e32 v1, 0xc80, v3
	v_lshl_add_u32 v1, v167, 1, v1
	v_add_u32_e32 v1, 0x18000, v1
	v_mov_b32_e32 v167, v39
	v_mov_b32_e32 v90, 0
	v_mov_b32_e32 v91, 0
	v_mov_b32_e32 v92, 0
	v_mov_b32_e32 v93, 0
	v_mov_b32_e32 v94, 0
	v_mov_b32_e32 v95, 0
	v_mov_b32_e32 v96, 0
	v_mov_b32_e32 v97, 0
	v_mov_b32_e32 v98, 0
	v_mov_b32_e32 v99, 0
	v_mov_b32_e32 v100, 0
	v_mov_b32_e32 v101, 0
	ds_read_b128 v[46:49], v166 offset:2048
	ds_read_b128 v[14:17], v166 offset:0
	ds_read_b128 v[30:33], v166 offset:1024
	ds_read_b128 v[62:65], v166 offset:3072
	s_waitcnt vmcnt(14) lgkmcnt(3)
	v_mfma_f32_32x32x16_f16 v[34:49], v[46:49], v[106:109], 0
	s_waitcnt lgkmcnt(2)
	v_mfma_f32_32x32x16_f16 v[2:17], v[14:17], v[102:105], 0
	s_waitcnt lgkmcnt(1)
	v_mfma_f32_32x32x16_f16 v[18:33], v[30:33], v[102:105], 0
	s_waitcnt lgkmcnt(0)
	v_mfma_f32_32x32x16_f16 v[50:65], v[62:65], v[106:109], 0
	ds_write_b128 v167, v[66:69] offset:32768
	ds_write_b128 v167, v[70:73] offset:32784
	ds_write_b128 v167, v[74:77] offset:32800
	ds_write_b128 v167, v[78:81] offset:32816
	s_lshl_b32 s22, s42, 2
	s_cmpk_lt_u32 s49, 0x100
	s_cselect_b32 s20, s14, s10
	s_cselect_b32 s21, s15, s11
	s_cselect_b32 s22, s22, 0
	s_cselect_b32 s23, 0xff, 15
	v_and_b32_e32 v82, s23, v0
	v_lshlrev_b32_e32 v82, 4, v82
	v_add_u32_e32 v82, s22, v82
	global_load_dwordx4 v[102:105], v82, s[20:21]
	s_nop 7
	ds_read_b128 v[46:49], v166 offset:6144
	ds_read_b128 v[14:17], v166 offset:4096
	ds_read_b128 v[30:33], v166 offset:5120
	ds_read_b128 v[62:65], v166 offset:7168
	v_pk_mul_f32 v[66:67], v[34:35], v[18:19]
	v_pk_mul_f32 v[68:69], v[36:37], v[20:21]
	v_pk_mul_f32 v[70:71], v[38:39], v[22:23]
	v_pk_mul_f32 v[72:73], v[40:41], v[24:25]
	v_pk_mul_f32 v[74:75], v[42:43], v[26:27]
	v_pk_mul_f32 v[76:77], v[44:45], v[28:29]
	s_waitcnt vmcnt(13) lgkmcnt(3)
	v_mfma_f32_32x32x16_f16 v[34:49], v[46:49], v[114:117], 0
	v_pk_fma_f32 v[66:67], v[2:3], v[50:51], v[66:67]
	v_pk_fma_f32 v[68:69], v[4:5], v[52:53], v[68:69]
	v_pk_fma_f32 v[70:71], v[6:7], v[54:55], v[70:71]
	v_pk_fma_f32 v[72:73], v[8:9], v[56:57], v[72:73]
	v_pk_fma_f32 v[74:75], v[10:11], v[58:59], v[74:75]
	v_pk_fma_f32 v[76:77], v[12:13], v[60:61], v[76:77]
	s_waitcnt lgkmcnt(2)
	v_mfma_f32_32x32x16_f16 v[2:17], v[14:17], v[110:113], 0
	v_pk_mul_f32 v[78:79], v[18:19], v[50:51]
	v_pk_mul_f32 v[80:81], v[20:21], v[52:53]
	v_pk_mul_f32 v[82:83], v[22:23], v[54:55]
	v_pk_mul_f32 v[84:85], v[24:25], v[56:57]
	v_pk_mul_f32 v[86:87], v[26:27], v[58:59]
	v_pk_mul_f32 v[88:89], v[28:29], v[60:61]
	s_waitcnt lgkmcnt(1)
	v_mfma_f32_32x32x16_f16 v[18:33], v[30:33], v[110:113], 0
	s_waitcnt lgkmcnt(0)
	v_mfma_f32_32x32x16_f16 v[50:65], v[62:65], v[114:117], 0
	v_rcp_f32_e32 v78, v78
	v_rcp_f32_e32 v79, v79
	v_rcp_f32_e32 v80, v80
	v_rcp_f32_e32 v81, v81
	v_rcp_f32_e32 v82, v82
	v_rcp_f32_e32 v83, v83
	v_rcp_f32_e32 v84, v84
	v_rcp_f32_e32 v85, v85
	v_rcp_f32_e32 v86, v86
	v_rcp_f32_e32 v87, v87
	v_rcp_f32_e32 v88, v88
	v_rcp_f32_e32 v89, v89
	v_pk_fma_f32 v[90:91], v[66:67], v[78:79], v[90:91]
	v_pk_fma_f32 v[92:93], v[68:69], v[80:81], v[92:93]
	v_pk_fma_f32 v[94:95], v[70:71], v[82:83], v[94:95]
	v_pk_fma_f32 v[96:97], v[72:73], v[84:85], v[96:97]
	v_pk_fma_f32 v[98:99], v[74:75], v[86:87], v[98:99]
	v_pk_fma_f32 v[100:101], v[76:77], v[88:89], v[100:101]
	ds_read_b128 v[46:49], v166 offset:10240
	ds_read_b128 v[14:17], v166 offset:8192
	ds_read_b128 v[30:33], v166 offset:9216
	ds_read_b128 v[62:65], v166 offset:11264
	v_pk_mul_f32 v[66:67], v[34:35], v[18:19]
	v_pk_mul_f32 v[68:69], v[36:37], v[20:21]
	v_pk_mul_f32 v[70:71], v[38:39], v[22:23]
	v_pk_mul_f32 v[72:73], v[40:41], v[24:25]
	v_pk_mul_f32 v[74:75], v[42:43], v[26:27]
	v_pk_mul_f32 v[76:77], v[44:45], v[28:29]
	s_waitcnt vmcnt(11) lgkmcnt(3)
	v_mfma_f32_32x32x16_f16 v[34:49], v[46:49], v[122:125], 0
	v_pk_fma_f32 v[66:67], v[2:3], v[50:51], v[66:67]
	v_pk_fma_f32 v[68:69], v[4:5], v[52:53], v[68:69]
	v_pk_fma_f32 v[70:71], v[6:7], v[54:55], v[70:71]
	v_pk_fma_f32 v[72:73], v[8:9], v[56:57], v[72:73]
	v_pk_fma_f32 v[74:75], v[10:11], v[58:59], v[74:75]
	v_pk_fma_f32 v[76:77], v[12:13], v[60:61], v[76:77]
	s_waitcnt lgkmcnt(2)
	v_mfma_f32_32x32x16_f16 v[2:17], v[14:17], v[118:121], 0
	v_pk_mul_f32 v[78:79], v[18:19], v[50:51]
	v_pk_mul_f32 v[80:81], v[20:21], v[52:53]
	v_pk_mul_f32 v[82:83], v[22:23], v[54:55]
	v_pk_mul_f32 v[84:85], v[24:25], v[56:57]
	v_pk_mul_f32 v[86:87], v[26:27], v[58:59]
	v_pk_mul_f32 v[88:89], v[28:29], v[60:61]
	s_waitcnt lgkmcnt(1)
	v_mfma_f32_32x32x16_f16 v[18:33], v[30:33], v[118:121], 0
	s_waitcnt lgkmcnt(0)
	v_mfma_f32_32x32x16_f16 v[50:65], v[62:65], v[122:125], 0
	v_rcp_f32_e32 v78, v78
	v_rcp_f32_e32 v79, v79
	v_rcp_f32_e32 v80, v80
	v_rcp_f32_e32 v81, v81
	v_rcp_f32_e32 v82, v82
	v_rcp_f32_e32 v83, v83
	v_rcp_f32_e32 v84, v84
	v_rcp_f32_e32 v85, v85
	v_rcp_f32_e32 v86, v86
	v_rcp_f32_e32 v87, v87
	v_rcp_f32_e32 v88, v88
	v_rcp_f32_e32 v89, v89
	v_pk_fma_f32 v[90:91], v[66:67], v[78:79], v[90:91]
	v_pk_fma_f32 v[92:93], v[68:69], v[80:81], v[92:93]
	v_pk_fma_f32 v[94:95], v[70:71], v[82:83], v[94:95]
	v_pk_fma_f32 v[96:97], v[72:73], v[84:85], v[96:97]
	v_pk_fma_f32 v[98:99], v[74:75], v[86:87], v[98:99]
	v_pk_fma_f32 v[100:101], v[76:77], v[88:89], v[100:101]
	ds_read_b128 v[46:49], v166 offset:14336
	ds_read_b128 v[14:17], v166 offset:12288
	ds_read_b128 v[30:33], v166 offset:13312
	ds_read_b128 v[62:65], v166 offset:15360
	v_pk_mul_f32 v[66:67], v[34:35], v[18:19]
	v_pk_mul_f32 v[68:69], v[36:37], v[20:21]
	v_pk_mul_f32 v[70:71], v[38:39], v[22:23]
	v_pk_mul_f32 v[72:73], v[40:41], v[24:25]
	v_pk_mul_f32 v[74:75], v[42:43], v[26:27]
	v_pk_mul_f32 v[76:77], v[44:45], v[28:29]
	s_waitcnt vmcnt(9) lgkmcnt(3)
	v_mfma_f32_32x32x16_f16 v[34:49], v[46:49], v[130:133], 0
	v_pk_fma_f32 v[66:67], v[2:3], v[50:51], v[66:67]
	v_pk_fma_f32 v[68:69], v[4:5], v[52:53], v[68:69]
	v_pk_fma_f32 v[70:71], v[6:7], v[54:55], v[70:71]
	v_pk_fma_f32 v[72:73], v[8:9], v[56:57], v[72:73]
	v_pk_fma_f32 v[74:75], v[10:11], v[58:59], v[74:75]
	v_pk_fma_f32 v[76:77], v[12:13], v[60:61], v[76:77]
	s_waitcnt lgkmcnt(2)
	v_mfma_f32_32x32x16_f16 v[2:17], v[14:17], v[126:129], 0
	v_pk_mul_f32 v[78:79], v[18:19], v[50:51]
	v_pk_mul_f32 v[80:81], v[20:21], v[52:53]
	v_pk_mul_f32 v[82:83], v[22:23], v[54:55]
	v_pk_mul_f32 v[84:85], v[24:25], v[56:57]
	v_pk_mul_f32 v[86:87], v[26:27], v[58:59]
	v_pk_mul_f32 v[88:89], v[28:29], v[60:61]
	s_waitcnt lgkmcnt(1)
	v_mfma_f32_32x32x16_f16 v[18:33], v[30:33], v[126:129], 0
	s_waitcnt lgkmcnt(0)
	v_mfma_f32_32x32x16_f16 v[50:65], v[62:65], v[130:133], 0
	v_rcp_f32_e32 v78, v78
	v_rcp_f32_e32 v79, v79
	v_rcp_f32_e32 v80, v80
	v_rcp_f32_e32 v81, v81
	v_rcp_f32_e32 v82, v82
	v_rcp_f32_e32 v83, v83
	v_rcp_f32_e32 v84, v84
	v_rcp_f32_e32 v85, v85
	v_rcp_f32_e32 v86, v86
	v_rcp_f32_e32 v87, v87
	v_rcp_f32_e32 v88, v88
	v_rcp_f32_e32 v89, v89
	v_pk_fma_f32 v[90:91], v[66:67], v[78:79], v[90:91]
	v_pk_fma_f32 v[92:93], v[68:69], v[80:81], v[92:93]
	v_pk_fma_f32 v[94:95], v[70:71], v[82:83], v[94:95]
	v_pk_fma_f32 v[96:97], v[72:73], v[84:85], v[96:97]
	v_pk_fma_f32 v[98:99], v[74:75], v[86:87], v[98:99]
	v_pk_fma_f32 v[100:101], v[76:77], v[88:89], v[100:101]
	ds_read_b128 v[46:49], v166 offset:18432
	ds_read_b128 v[14:17], v166 offset:16384
	ds_read_b128 v[30:33], v166 offset:17408
	ds_read_b128 v[62:65], v166 offset:19456
	v_pk_mul_f32 v[66:67], v[34:35], v[18:19]
	v_pk_mul_f32 v[68:69], v[36:37], v[20:21]
	v_pk_mul_f32 v[70:71], v[38:39], v[22:23]
	v_pk_mul_f32 v[72:73], v[40:41], v[24:25]
	v_pk_mul_f32 v[74:75], v[42:43], v[26:27]
	v_pk_mul_f32 v[76:77], v[44:45], v[28:29]
	s_waitcnt vmcnt(7) lgkmcnt(3)
	v_mfma_f32_32x32x16_f16 v[34:49], v[46:49], v[138:141], 0
	v_pk_fma_f32 v[66:67], v[2:3], v[50:51], v[66:67]
	v_pk_fma_f32 v[68:69], v[4:5], v[52:53], v[68:69]
	v_pk_fma_f32 v[70:71], v[6:7], v[54:55], v[70:71]
	v_pk_fma_f32 v[72:73], v[8:9], v[56:57], v[72:73]
	v_pk_fma_f32 v[74:75], v[10:11], v[58:59], v[74:75]
	v_pk_fma_f32 v[76:77], v[12:13], v[60:61], v[76:77]
	s_waitcnt lgkmcnt(2)
	v_mfma_f32_32x32x16_f16 v[2:17], v[14:17], v[134:137], 0
	v_pk_mul_f32 v[78:79], v[18:19], v[50:51]
	v_pk_mul_f32 v[80:81], v[20:21], v[52:53]
	v_pk_mul_f32 v[82:83], v[22:23], v[54:55]
	v_pk_mul_f32 v[84:85], v[24:25], v[56:57]
	v_pk_mul_f32 v[86:87], v[26:27], v[58:59]
	v_pk_mul_f32 v[88:89], v[28:29], v[60:61]
	s_waitcnt lgkmcnt(1)
	v_mfma_f32_32x32x16_f16 v[18:33], v[30:33], v[134:137], 0
	s_waitcnt lgkmcnt(0)
	v_mfma_f32_32x32x16_f16 v[50:65], v[62:65], v[138:141], 0
	v_rcp_f32_e32 v78, v78
	v_rcp_f32_e32 v79, v79
	v_rcp_f32_e32 v80, v80
	v_rcp_f32_e32 v81, v81
	v_rcp_f32_e32 v82, v82
	v_rcp_f32_e32 v83, v83
	v_rcp_f32_e32 v84, v84
	v_rcp_f32_e32 v85, v85
	v_rcp_f32_e32 v86, v86
	v_rcp_f32_e32 v87, v87
	v_rcp_f32_e32 v88, v88
	v_rcp_f32_e32 v89, v89
	v_pk_fma_f32 v[90:91], v[66:67], v[78:79], v[90:91]
	v_pk_fma_f32 v[92:93], v[68:69], v[80:81], v[92:93]
	v_pk_fma_f32 v[94:95], v[70:71], v[82:83], v[94:95]
	v_pk_fma_f32 v[96:97], v[72:73], v[84:85], v[96:97]
	v_pk_fma_f32 v[98:99], v[74:75], v[86:87], v[98:99]
	v_pk_fma_f32 v[100:101], v[76:77], v[88:89], v[100:101]
	ds_read_b128 v[46:49], v166 offset:22528
	ds_read_b128 v[14:17], v166 offset:20480
	ds_read_b128 v[30:33], v166 offset:21504
	ds_read_b128 v[62:65], v166 offset:23552
	v_pk_mul_f32 v[66:67], v[34:35], v[18:19]
	v_pk_mul_f32 v[68:69], v[36:37], v[20:21]
	v_pk_mul_f32 v[70:71], v[38:39], v[22:23]
	v_pk_mul_f32 v[72:73], v[40:41], v[24:25]
	v_pk_mul_f32 v[74:75], v[42:43], v[26:27]
	v_pk_mul_f32 v[76:77], v[44:45], v[28:29]
	s_waitcnt vmcnt(5) lgkmcnt(3)
	v_mfma_f32_32x32x16_f16 v[34:49], v[46:49], v[146:149], 0
	v_pk_fma_f32 v[66:67], v[2:3], v[50:51], v[66:67]
	v_pk_fma_f32 v[68:69], v[4:5], v[52:53], v[68:69]
	v_pk_fma_f32 v[70:71], v[6:7], v[54:55], v[70:71]
	v_pk_fma_f32 v[72:73], v[8:9], v[56:57], v[72:73]
	v_pk_fma_f32 v[74:75], v[10:11], v[58:59], v[74:75]
	v_pk_fma_f32 v[76:77], v[12:13], v[60:61], v[76:77]
	s_waitcnt lgkmcnt(2)
	v_mfma_f32_32x32x16_f16 v[2:17], v[14:17], v[142:145], 0
	v_pk_mul_f32 v[78:79], v[18:19], v[50:51]
	v_pk_mul_f32 v[80:81], v[20:21], v[52:53]
	v_pk_mul_f32 v[82:83], v[22:23], v[54:55]
	v_pk_mul_f32 v[84:85], v[24:25], v[56:57]
	v_pk_mul_f32 v[86:87], v[26:27], v[58:59]
	v_pk_mul_f32 v[88:89], v[28:29], v[60:61]
	s_waitcnt lgkmcnt(1)
	v_mfma_f32_32x32x16_f16 v[18:33], v[30:33], v[142:145], 0
	s_waitcnt lgkmcnt(0)
	v_mfma_f32_32x32x16_f16 v[50:65], v[62:65], v[146:149], 0
	v_rcp_f32_e32 v78, v78
	v_rcp_f32_e32 v79, v79
	v_rcp_f32_e32 v80, v80
	v_rcp_f32_e32 v81, v81
	v_rcp_f32_e32 v82, v82
	v_rcp_f32_e32 v83, v83
	v_rcp_f32_e32 v84, v84
	v_rcp_f32_e32 v85, v85
	v_rcp_f32_e32 v86, v86
	v_rcp_f32_e32 v87, v87
	v_rcp_f32_e32 v88, v88
	v_rcp_f32_e32 v89, v89
	v_pk_fma_f32 v[90:91], v[66:67], v[78:79], v[90:91]
	v_pk_fma_f32 v[92:93], v[68:69], v[80:81], v[92:93]
	v_pk_fma_f32 v[94:95], v[70:71], v[82:83], v[94:95]
	v_pk_fma_f32 v[96:97], v[72:73], v[84:85], v[96:97]
	v_pk_fma_f32 v[98:99], v[74:75], v[86:87], v[98:99]
	v_pk_fma_f32 v[100:101], v[76:77], v[88:89], v[100:101]
	ds_read_b128 v[46:49], v166 offset:26624
	ds_read_b128 v[14:17], v166 offset:24576
	ds_read_b128 v[30:33], v166 offset:25600
	ds_read_b128 v[62:65], v166 offset:27648
	v_pk_mul_f32 v[66:67], v[34:35], v[18:19]
	v_pk_mul_f32 v[68:69], v[36:37], v[20:21]
	v_pk_mul_f32 v[70:71], v[38:39], v[22:23]
	v_pk_mul_f32 v[72:73], v[40:41], v[24:25]
	v_pk_mul_f32 v[74:75], v[42:43], v[26:27]
	v_pk_mul_f32 v[76:77], v[44:45], v[28:29]
	s_waitcnt vmcnt(3) lgkmcnt(3)
	v_mfma_f32_32x32x16_f16 v[34:49], v[46:49], v[154:157], 0
	v_pk_fma_f32 v[66:67], v[2:3], v[50:51], v[66:67]
	v_pk_fma_f32 v[68:69], v[4:5], v[52:53], v[68:69]
	v_pk_fma_f32 v[70:71], v[6:7], v[54:55], v[70:71]
	v_pk_fma_f32 v[72:73], v[8:9], v[56:57], v[72:73]
	v_pk_fma_f32 v[74:75], v[10:11], v[58:59], v[74:75]
	v_pk_fma_f32 v[76:77], v[12:13], v[60:61], v[76:77]
	s_waitcnt lgkmcnt(2)
	v_mfma_f32_32x32x16_f16 v[2:17], v[14:17], v[150:153], 0
	v_pk_mul_f32 v[78:79], v[18:19], v[50:51]
	v_pk_mul_f32 v[80:81], v[20:21], v[52:53]
	v_pk_mul_f32 v[82:83], v[22:23], v[54:55]
	v_pk_mul_f32 v[84:85], v[24:25], v[56:57]
	v_pk_mul_f32 v[86:87], v[26:27], v[58:59]
	v_pk_mul_f32 v[88:89], v[28:29], v[60:61]
	s_waitcnt lgkmcnt(1)
	v_mfma_f32_32x32x16_f16 v[18:33], v[30:33], v[150:153], 0
	s_waitcnt lgkmcnt(0)
	v_mfma_f32_32x32x16_f16 v[50:65], v[62:65], v[154:157], 0
	v_rcp_f32_e32 v78, v78
	v_rcp_f32_e32 v79, v79
	v_rcp_f32_e32 v80, v80
	v_rcp_f32_e32 v81, v81
	v_rcp_f32_e32 v82, v82
	v_rcp_f32_e32 v83, v83
	v_rcp_f32_e32 v84, v84
	v_rcp_f32_e32 v85, v85
	v_rcp_f32_e32 v86, v86
	v_rcp_f32_e32 v87, v87
	v_rcp_f32_e32 v88, v88
	v_rcp_f32_e32 v89, v89
	v_pk_fma_f32 v[90:91], v[66:67], v[78:79], v[90:91]
	v_pk_fma_f32 v[92:93], v[68:69], v[80:81], v[92:93]
	v_pk_fma_f32 v[94:95], v[70:71], v[82:83], v[94:95]
	v_pk_fma_f32 v[96:97], v[72:73], v[84:85], v[96:97]
	v_pk_fma_f32 v[98:99], v[74:75], v[86:87], v[98:99]
	v_pk_fma_f32 v[100:101], v[76:77], v[88:89], v[100:101]
	ds_read_b128 v[46:49], v166 offset:30720
	ds_read_b128 v[14:17], v166 offset:28672
	ds_read_b128 v[30:33], v166 offset:29696
	ds_read_b128 v[62:65], v166 offset:31744
	v_pk_mul_f32 v[66:67], v[34:35], v[18:19]
	v_pk_mul_f32 v[68:69], v[36:37], v[20:21]
	v_pk_mul_f32 v[70:71], v[38:39], v[22:23]
	v_pk_mul_f32 v[72:73], v[40:41], v[24:25]
	v_pk_mul_f32 v[74:75], v[42:43], v[26:27]
	v_pk_mul_f32 v[76:77], v[44:45], v[28:29]
	s_waitcnt vmcnt(1) lgkmcnt(3)
	v_mfma_f32_32x32x16_f16 v[34:49], v[46:49], v[162:165], 0
	v_pk_fma_f32 v[66:67], v[2:3], v[50:51], v[66:67]
	v_pk_fma_f32 v[68:69], v[4:5], v[52:53], v[68:69]
	v_pk_fma_f32 v[70:71], v[6:7], v[54:55], v[70:71]
	v_pk_fma_f32 v[72:73], v[8:9], v[56:57], v[72:73]
	v_pk_fma_f32 v[74:75], v[10:11], v[58:59], v[74:75]
	v_pk_fma_f32 v[76:77], v[12:13], v[60:61], v[76:77]
	s_waitcnt lgkmcnt(2)
	v_mfma_f32_32x32x16_f16 v[2:17], v[14:17], v[158:161], 0
	v_pk_mul_f32 v[78:79], v[18:19], v[50:51]
	v_pk_mul_f32 v[80:81], v[20:21], v[52:53]
	v_pk_mul_f32 v[82:83], v[22:23], v[54:55]
	v_pk_mul_f32 v[84:85], v[24:25], v[56:57]
	v_pk_mul_f32 v[86:87], v[26:27], v[58:59]
	v_pk_mul_f32 v[88:89], v[28:29], v[60:61]
	s_waitcnt lgkmcnt(1)
	v_mfma_f32_32x32x16_f16 v[18:33], v[30:33], v[158:161], 0
	s_waitcnt lgkmcnt(0)
	v_mfma_f32_32x32x16_f16 v[50:65], v[62:65], v[162:165], 0
	v_rcp_f32_e32 v78, v78
	v_rcp_f32_e32 v79, v79
	v_rcp_f32_e32 v80, v80
	v_rcp_f32_e32 v81, v81
	v_rcp_f32_e32 v82, v82
	v_rcp_f32_e32 v83, v83
	v_rcp_f32_e32 v84, v84
	v_rcp_f32_e32 v85, v85
	v_rcp_f32_e32 v86, v86
	v_rcp_f32_e32 v87, v87
	v_rcp_f32_e32 v88, v88
	v_rcp_f32_e32 v89, v89
	v_pk_fma_f32 v[90:91], v[66:67], v[78:79], v[90:91]
	v_pk_fma_f32 v[92:93], v[68:69], v[80:81], v[92:93]
	v_pk_fma_f32 v[94:95], v[70:71], v[82:83], v[94:95]
	v_pk_fma_f32 v[96:97], v[72:73], v[84:85], v[96:97]
	v_pk_fma_f32 v[98:99], v[74:75], v[86:87], v[98:99]
	v_pk_fma_f32 v[100:101], v[76:77], v[88:89], v[100:101]
	v_pk_mul_f32 v[66:67], v[34:35], v[18:19]
	v_pk_mul_f32 v[68:69], v[36:37], v[20:21]
	v_pk_mul_f32 v[70:71], v[38:39], v[22:23]
	v_pk_mul_f32 v[72:73], v[40:41], v[24:25]
	v_pk_mul_f32 v[74:75], v[42:43], v[26:27]
	v_pk_mul_f32 v[76:77], v[44:45], v[28:29]
	v_pk_fma_f32 v[66:67], v[2:3], v[50:51], v[66:67]
	v_pk_fma_f32 v[68:69], v[4:5], v[52:53], v[68:69]
	v_pk_fma_f32 v[70:71], v[6:7], v[54:55], v[70:71]
	v_pk_fma_f32 v[72:73], v[8:9], v[56:57], v[72:73]
	v_pk_fma_f32 v[74:75], v[10:11], v[58:59], v[74:75]
	v_pk_fma_f32 v[76:77], v[12:13], v[60:61], v[76:77]
	v_pk_mul_f32 v[78:79], v[18:19], v[50:51]
	v_pk_mul_f32 v[80:81], v[20:21], v[52:53]
	v_pk_mul_f32 v[82:83], v[22:23], v[54:55]
	v_pk_mul_f32 v[84:85], v[24:25], v[56:57]
	v_pk_mul_f32 v[86:87], v[26:27], v[58:59]
	v_pk_mul_f32 v[88:89], v[28:29], v[60:61]
	v_rcp_f32_e32 v78, v78
	v_rcp_f32_e32 v79, v79
	v_rcp_f32_e32 v80, v80
	v_rcp_f32_e32 v81, v81
	v_rcp_f32_e32 v82, v82
	v_rcp_f32_e32 v83, v83
	v_rcp_f32_e32 v84, v84
	v_rcp_f32_e32 v85, v85
	v_rcp_f32_e32 v86, v86
	v_rcp_f32_e32 v87, v87
	v_rcp_f32_e32 v88, v88
	v_rcp_f32_e32 v89, v89
	v_pk_fma_f32 v[90:91], v[66:67], v[78:79], v[90:91]
	v_pk_fma_f32 v[92:93], v[68:69], v[80:81], v[92:93]
	v_pk_fma_f32 v[94:95], v[70:71], v[82:83], v[94:95]
	v_pk_fma_f32 v[96:97], v[72:73], v[84:85], v[96:97]
	v_pk_fma_f32 v[98:99], v[74:75], v[86:87], v[98:99]
	v_pk_fma_f32 v[100:101], v[76:77], v[88:89], v[100:101]
	v_fma_f32 v66, v90, -2.0, s28
	v_subrev_f32_e32 v66, s29, v66
	v_mul_f32_e32 v66, 0x3fb8aa3b, v66
	v_exp_f32_e32 v66, v66
	v_fma_f32 v67, v91, -2.0, s28
	v_subrev_f32_e32 v67, s29, v67
	v_mul_f32_e32 v67, 0x3fb8aa3b, v67
	v_exp_f32_e32 v67, v67
	v_fma_f32 v68, v92, -2.0, s28
	v_subrev_f32_e32 v68, s29, v68
	v_mul_f32_e32 v68, 0x3fb8aa3b, v68
	v_exp_f32_e32 v68, v68
	v_fma_f32 v69, v93, -2.0, s28
	v_subrev_f32_e32 v69, s29, v69
	v_mul_f32_e32 v69, 0x3fb8aa3b, v69
	v_exp_f32_e32 v69, v69
	v_fma_f32 v70, v94, -2.0, s28
	v_subrev_f32_e32 v70, s29, v70
	v_mul_f32_e32 v70, 0x3fb8aa3b, v70
	v_exp_f32_e32 v70, v70
	v_fma_f32 v71, v95, -2.0, s28
	v_subrev_f32_e32 v71, s29, v71
	v_mul_f32_e32 v71, 0x3fb8aa3b, v71
	v_exp_f32_e32 v71, v71
	v_fma_f32 v72, v96, -2.0, s28
	v_subrev_f32_e32 v72, s29, v72
	v_mul_f32_e32 v72, 0x3fb8aa3b, v72
	v_exp_f32_e32 v72, v72
	v_fma_f32 v73, v97, -2.0, s28
	v_subrev_f32_e32 v73, s29, v73
	v_mul_f32_e32 v73, 0x3fb8aa3b, v73
	v_exp_f32_e32 v73, v73
	v_fma_f32 v74, v98, -2.0, s28
	v_subrev_f32_e32 v74, s29, v74
	v_mul_f32_e32 v74, 0x3fb8aa3b, v74
	v_exp_f32_e32 v74, v74
	v_fma_f32 v75, v99, -2.0, s28
	v_subrev_f32_e32 v75, s29, v75
	v_mul_f32_e32 v75, 0x3fb8aa3b, v75
	v_exp_f32_e32 v75, v75
	v_fma_f32 v76, v100, -2.0, s28
	v_subrev_f32_e32 v76, s29, v76
	v_mul_f32_e32 v76, 0x3fb8aa3b, v76
	v_exp_f32_e32 v76, v76
	v_fma_f32 v77, v101, -2.0, s28
	v_subrev_f32_e32 v77, s29, v77
	v_mul_f32_e32 v77, 0x3fb8aa3b, v77
	v_exp_f32_e32 v77, v77
	s_nop 0
	v_cvt_f16_f32_e32 v66, v66
	v_cvt_f16_f32_e32 v67, v67
	v_cvt_f16_f32_e32 v68, v68
	v_cvt_f16_f32_e32 v69, v69
	v_cvt_f16_f32_e32 v70, v70
	v_cvt_f16_f32_e32 v71, v71
	v_cvt_f16_f32_e32 v72, v72
	v_cvt_f16_f32_e32 v73, v73
	v_cvt_f16_f32_e32 v74, v74
	v_cvt_f16_f32_e32 v75, v75
	v_cvt_f16_f32_e32 v76, v76
	v_cvt_f16_f32_e32 v77, v77
	ds_write_b16 v1, v66
	ds_write_b16 v1, v67 offset:800
	ds_write_b16 v1, v68 offset:1600
	ds_write_b16 v1, v69 offset:2400
	ds_write_b16 v1, v70 offset:6400
	ds_write_b16 v1, v71 offset:7200
	ds_write_b16 v1, v72 offset:8000
	ds_write_b16 v1, v73 offset:8800
	ds_write_b16 v1, v74 offset:12800
	ds_write_b16 v1, v75 offset:13600
	ds_write_b16 v1, v76 offset:14400
	ds_write_b16 v1, v77 offset:15200
	s_cmpk_gt_u32 s49, 0xff
	s_cbranch_scc1 .Lf_wo_done
	s_waitcnt vmcnt(0)
	v_cvt_f16_f32_e32 v2, v102
	v_cvt_f16_f32_e32 v5, v105
	v_cvt_pk_f16_f32 v3, v103, v104
	v_pack_b32_f16 v2, v2, v3
	v_alignbit_b32 v3, v5, v3, 16
	v_and_b32_e32 v6, 0xff, v0
	v_lshlrev_b32_e32 v6, 3, v6
	s_lshl_b32 s22, s42, 1
	v_add_u32_e32 v6, s22, v6
	global_store_dwordx2 v6, v[2:3], s[18:19]

.Lf_pv:
	s_lshr_b32 s2, s49, 4
	s_and_b32 s2, s2, 16
	s_and_b32 s4, s51, 3
	v_and_b32_e32 v62, 15, v0
	s_cmp_lg_u32 s2, 0
	s_cselect_b32 s5, 7, 15
	v_and_b32_e32 v1, s5, v62
	v_or_b32_e32 v1, s2, v1
	v_mul_u32_u24_e32 v1, 0x320, v1
	v_and_b32_e32 v50, 48, v0
	s_mov_b32 s6, 0x18000
	v_add3_u32 v1, s6, v1, v50
	s_lshl_b32 s5, s4, 4
	v_or_b32_e32 v51, s5, v62
	v_mul_u32_u24_e32 v51, 0x320, v51
	s_mov_b32 s7, 0x8000
	v_add3_u32 v51, s7, v51, v50
	v_mov_b32_e32 v74, 0x3c003c00
	v_mov_b32_e32 v75, v74
	v_mov_b32_e32 v76, v74
	v_mov_b32_e32 v77, v74
	ds_read_b128 v[2:5], v1
	ds_read_b128 v[102:105], v51
	ds_read_b128 v[6:9], v1 offset:64
	ds_read_b128 v[106:109], v51 offset:64
	ds_read_b128 v[10:13], v1 offset:128
	ds_read_b128 v[110:113], v51 offset:128
	ds_read_b128 v[14:17], v1 offset:192
	ds_read_b128 v[114:117], v51 offset:192
	ds_read_b128 v[18:21], v1 offset:256
	ds_read_b128 v[118:121], v51 offset:256
	ds_read_b128 v[22:25], v1 offset:320
	ds_read_b128 v[122:125], v51 offset:320
	ds_read_b128 v[26:29], v1 offset:384
	ds_read_b128 v[126:129], v51 offset:384
	s_lshr_b32 s3, s43, 3
	s_mul_i32 s5, s3, 0x180
	s_add_i32 s5, s5, s41
	v_lshrrev_b32_e32 v78, 2, v0
	v_and_or_b32 v78, v78, 12, s2
	s_lshl_b32 s2, s33, 7
	s_and_b32 s2, s2, 0x380
	s_add_u32 s0, s62, s2
	s_addc_u32 s1, s63, 0
	s_lshl_b32 s2, s4, 5
	s_add_u32 s0, s0, s2
	s_addc_u32 s1, s1, 0
	v_add_u32_e32 v80, s5, v78
	v_mov_b32_e32 v81, 0
	v_lshlrev_b64 v[80:81], 10, v[80:81]
	v_lshlrev_b32_e32 v82, 1, v62
	v_mov_b32_e32 v83, 0
	v_lshl_add_u64 v[80:81], v[80:81], 0, v[82:83]
	v_lshl_add_u64 v[80:81], s[0:1], 0, v[80:81]
	s_waitcnt lgkmcnt(12)
	v_mfma_f32_16x16x32_f16 v[66:69], v[2:5], v[102:105], 0
	v_mfma_f32_16x16x32_f16 v[70:73], v[2:5], v[74:77], 0
	ds_read_b128 v[30:33], v1 offset:448
	ds_read_b128 v[130:133], v51 offset:448
	s_waitcnt lgkmcnt(12)
	v_mfma_f32_16x16x32_f16 v[66:69], v[6:9], v[106:109], v[66:69]
	v_mfma_f32_16x16x32_f16 v[70:73], v[6:9], v[74:77], v[70:73]
	ds_read_b128 v[34:37], v1 offset:512
	ds_read_b128 v[134:137], v51 offset:512
	s_waitcnt lgkmcnt(12)
	v_mfma_f32_16x16x32_f16 v[66:69], v[10:13], v[110:113], v[66:69]
	v_mfma_f32_16x16x32_f16 v[70:73], v[10:13], v[74:77], v[70:73]
	ds_read_b128 v[38:41], v1 offset:576
	ds_read_b128 v[138:141], v51 offset:576
	s_waitcnt lgkmcnt(12)
	v_mfma_f32_16x16x32_f16 v[66:69], v[14:17], v[114:117], v[66:69]
	v_mfma_f32_16x16x32_f16 v[70:73], v[14:17], v[74:77], v[70:73]
	ds_read_b128 v[42:45], v1 offset:640
	ds_read_b128 v[142:145], v51 offset:640
	s_waitcnt lgkmcnt(12)
	v_mfma_f32_16x16x32_f16 v[66:69], v[18:21], v[118:121], v[66:69]
	v_mfma_f32_16x16x32_f16 v[70:73], v[18:21], v[74:77], v[70:73]
	ds_read_b128 v[46:49], v1 offset:704
	ds_read_b128 v[146:149], v51 offset:704
	s_waitcnt lgkmcnt(12)
	v_mfma_f32_16x16x32_f16 v[66:69], v[22:25], v[122:125], v[66:69]
	v_mfma_f32_16x16x32_f16 v[70:73], v[22:25], v[74:77], v[70:73]
	s_waitcnt lgkmcnt(10)
	v_mfma_f32_16x16x32_f16 v[66:69], v[26:29], v[126:129], v[66:69]
	v_mfma_f32_16x16x32_f16 v[70:73], v[26:29], v[74:77], v[70:73]
	s_waitcnt lgkmcnt(8)
	v_mfma_f32_16x16x32_f16 v[66:69], v[30:33], v[130:133], v[66:69]
	v_mfma_f32_16x16x32_f16 v[70:73], v[30:33], v[74:77], v[70:73]
	s_waitcnt lgkmcnt(6)
	v_mfma_f32_16x16x32_f16 v[66:69], v[34:37], v[134:137], v[66:69]
	v_mfma_f32_16x16x32_f16 v[70:73], v[34:37], v[74:77], v[70:73]
	s_waitcnt lgkmcnt(4)
	v_mfma_f32_16x16x32_f16 v[66:69], v[38:41], v[138:141], v[66:69]
	v_mfma_f32_16x16x32_f16 v[70:73], v[38:41], v[74:77], v[70:73]
	s_waitcnt lgkmcnt(2)
	v_mfma_f32_16x16x32_f16 v[66:69], v[42:45], v[142:145], v[66:69]
	v_mfma_f32_16x16x32_f16 v[70:73], v[42:45], v[74:77], v[70:73]
	s_waitcnt lgkmcnt(0)
	v_mfma_f32_16x16x32_f16 v[66:69], v[46:49], v[146:149], v[66:69]
	v_mfma_f32_16x16x32_f16 v[70:73], v[46:49], v[74:77], v[70:73]
	v_cmp_gt_u32_e64 s[0:1], 24, v78
	s_nop 7
	v_div_scale_f32 v84, s[6:7], v70, v70, 1.0
	v_div_scale_f32 v85, s[6:7], v71, v71, 1.0
	v_div_scale_f32 v86, s[6:7], v72, v72, 1.0
	v_div_scale_f32 v87, s[6:7], v73, v73, 1.0
	v_rcp_f32_e32 v88, v84
	v_rcp_f32_e32 v89, v85
	v_rcp_f32_e32 v90, v86
	v_rcp_f32_e32 v91, v87
	v_div_scale_f32 v92, s[10:11], 1.0, v70, 1.0
	v_div_scale_f32 v93, s[12:13], 1.0, v71, 1.0
	v_div_scale_f32 v94, s[14:15], 1.0, v72, 1.0
	v_div_scale_f32 v95, s[16:17], 1.0, v73, 1.0
	v_fma_f32 v96, -v84, v88, 1.0
	v_fma_f32 v97, -v85, v89, 1.0
	v_fma_f32 v98, -v86, v90, 1.0
	v_fma_f32 v99, -v87, v91, 1.0
	v_fmac_f32_e32 v88, v96, v88
	v_fmac_f32_e32 v89, v97, v89
	v_fmac_f32_e32 v90, v98, v90
	v_fmac_f32_e32 v91, v99, v91
	v_mul_f32_e32 v100, v92, v88
	v_mul_f32_e32 v101, v93, v89
	v_mul_f32_e32 v102, v94, v90
	v_mul_f32_e32 v103, v95, v91
	v_fma_f32 v96, -v84, v100, v92
	v_fma_f32 v97, -v85, v101, v93
	v_fma_f32 v98, -v86, v102, v94
	v_fma_f32 v99, -v87, v103, v95
	v_fmac_f32_e32 v100, v96, v88
	v_fmac_f32_e32 v101, v97, v89
	v_fmac_f32_e32 v102, v98, v90
	v_fmac_f32_e32 v103, v99, v91
	v_fma_f32 v84, -v84, v100, v92
	v_fma_f32 v85, -v85, v101, v93
	v_fma_f32 v86, -v86, v102, v94
	v_fma_f32 v87, -v87, v103, v95
	s_mov_b64 vcc, s[10:11]
	s_nop 3
	v_div_fmas_f32 v84, v84, v88, v100
	s_mov_b64 vcc, s[12:13]
	s_nop 3
	v_div_fmas_f32 v85, v85, v89, v101
	s_mov_b64 vcc, s[14:15]
	s_nop 3
	v_div_fmas_f32 v86, v86, v90, v102
	s_mov_b64 vcc, s[16:17]
	s_nop 3
	v_div_fmas_f32 v87, v87, v91, v103
	v_div_fixup_f32 v84, v84, v70, 1.0
	v_div_fixup_f32 v85, v85, v71, 1.0
	v_div_fixup_f32 v86, v86, v72, 1.0
	v_div_fixup_f32 v87, v87, v73, 1.0
	v_fma_mixlo_f16 v66, v66, v84, 0
	v_fma_mixlo_f16 v67, v67, v85, 0
	v_fma_mixlo_f16 v68, v68, v86, 0
	v_fma_mixlo_f16 v69, v69, v87, 0
	s_and_saveexec_b64 s[2:3], s[0:1]
	global_store_short v[80:81], v66, off
	global_store_short v[80:81], v67, off offset:1024
	global_store_short v[80:81], v68, off offset:2048
	global_store_short v[80:81], v69, off offset:3072
	s_endpgm
